# speedup vs baseline: 1.0074x; 1.0074x over previous
.LBB3_33:
	s_or_b64 exec, exec, s[12:13]
	s_load_dwordx2 s[0:1], s[0:1], 0x30
	s_waitcnt vmcnt(0)
	v_add_u32_e32 v2, s22, v12
	v_or_b32_e32 v2, v2, v14
	v_ashrrev_i32_e32 v3, 31, v2
	v_lshl_add_u64 v[174:175], v[2:3], 4, s[20:21]
	v_and_b32_e32 v2, 48, v0
	s_lshl_b32 s37, s29, 8
	v_lshlrev_b32_e32 v187, 13, v1
	s_lshl_b32 s42, s29, 15
	s_add_i32 s42, s42, 0x630100
	v_lshrrev_b32_e32 v186, 1, v187
	v_add3_u32 v186, v186, v170, s42
	v_lshl_or_b32 v2, v1, 8, v2
	v_lshl_or_b32 v184, v1, 5, s37
	v_add_u32_e32 v1, 0x2000, v187
	v_and_b32_e32 v188, 0xe000, v1
	v_add_u32_e32 v1, 0x4000, v187
	s_ashr_i32 s23, s22, 31
	v_and_b32_e32 v189, 0xe000, v1
	v_add_u32_e32 v1, 0x6000, v187
	s_and_b32 s17, s9, 0xffff
	s_lshl_b64 s[2:3], s[22:23], 1
	v_and_b32_e32 v190, 0xe000, v1
	v_add_u32_e32 v1, 0xa000, v187
	v_and_b32_e32 v0, 31, v0
	v_mov_b32_e32 v177, 0
	s_add_u32 s2, s8, s2
	v_and_b32_e32 v191, 0xe000, v1
	v_add_u32_e32 v1, 0xc000, v187
	s_mov_b32 s16, s8
	v_or_b32_e32 v169, s30, v11
	v_lshlrev_b32_e32 v176, 2, v0
	v_lshlrev_b32_e32 v0, 3, v10
	s_addc_u32 s3, s9, s3
	v_mov_b32_e32 v7, v177
	v_mov_b32_e32 v13, v177
	v_and_b32_e32 v192, 0xe000, v1
	v_add_u32_e32 v1, 0xe000, v187
	s_lshl_b32 s8, s28, 3
	s_mov_b32 s19, 0x20000
	s_mov_b32 s18, 0x6b0100
	v_lshl_add_u64 v[178:179], s[10:11], 0, v[176:177]
	v_add_u32_e32 v185, s30, v10
	s_mov_b32 s36, 1
	v_lshl_add_u64 v[180:181], s[2:3], 0, v[6:7]
	v_lshl_add_u64 v[182:183], s[10:11], 0, v[12:13]
	v_cmp_eq_u32_e64 s[2:3], 0, v10
	v_and_b32_e32 v193, 0xe000, v1
	s_add_i32 s37, s37, s8
	v_xor_b32_e32 v194, 0x8000, v187
	s_mov_b64 s[8:9], 0
	s_mov_b32 s38, 0x186a0
	s_mov_b32 s39, 0x40004000
	s_mov_b32 s40, 0xbb8000
	v_add_u32_e32 v195, v15, v0
	v_mov_b32_e32 v196, 1
	v_mov_b32_e32 v0, v177
	v_mov_b32_e32 v1, v177
	v_mov_b32_e32 v2, v177
	v_mov_b32_e32 v3, v177
	v_mov_b32_e32 v4, v177
	v_mov_b32_e32 v5, v177
	v_mov_b32_e32 v6, v177
	s_waitcnt lgkmcnt(0)
	v_mov_b32_e32 v8, v177
	v_mov_b32_e32 v9, v177
	v_mov_b32_e32 v10, v177
	v_mov_b32_e32 v11, v177
	v_mov_b32_e32 v12, v177
	v_mov_b32_e32 v14, v177
	v_mov_b32_e32 v15, v177
	v_add_u32_e32 v206, 0x80, v169
	v_mov_b32_e32 v207, 0
	v_lshlrev_b64 v[206:207], 14, v[206:207]
	v_lshl_add_u64 v[206:207], v[174:175], 0, v[206:207]
	global_load_dwordx4 v[160:163], v[206:207], off nt
	v_readfirstlane_b32 s42, v187
	s_cmp_lt_u32 s42, 0x8000
	s_cbranch_scc1 .Lrec_noprio
	s_setprio 1
.Lrec_noprio:
.Lrec_loop:
	s_add_i32 s10, s36, -1
	s_and_b32 s54, s10, 1
	v_lshl_add_u32 v164, s54, 18, v186
	s_bfe_u32 s54, s10, 0x10001
	s_mul_i32 s54, s54, 0x40004000
	s_sleep 10
	buffer_load_dwordx4 v[16:19], v164, s[16:19], 0 offen sc1
	buffer_load_dwordx4 v[20:23], v164, s[16:19], 0 offen offset:1024 sc1
	buffer_load_dwordx4 v[24:27], v164, s[16:19], 0 offen offset:2048 sc1
	buffer_load_dwordx4 v[28:31], v164, s[16:19], 0 offen offset:3072 sc1
	s_lshl_b32 s41, s36, 7
	s_mov_b32 s43, 0
	s_mov_b32 s45, 15
	s_mov_b32 s46, 0
	s_mov_b32 s55, 0
	s_add_i32 s11, s41, 0x80
	v_add_u32_e32 v206, s11, v169
	v_mov_b32_e32 v207, 0
	v_lshlrev_b64 v[206:207], 14, v[206:207]
	v_lshl_add_u64 v[206:207], v[174:175], 0, v[206:207]
	s_lshl_b32 s11, s36, 16
	s_and_b32 s11, s11, 0x10000
	v_add_u32_e32 v173, s11, v170
	s_waitcnt vmcnt(3)
	v_xor_b32_e32 v16, s54, v16
	v_xor_b32_e32 v17, s54, v17
	v_xor_b32_e32 v18, s54, v18
	v_xor_b32_e32 v19, s54, v19
	v_or3_b32 v0, v16, v17, v18
	v_bitop3_b32 v0, v0, s39, v19 bitop3:0xc8
	v_cmp_ne_u32_e32 vcc, 0, v0
	s_cmp_lg_u64 vcc, 0
	s_cbranch_scc1 .Lrec_e0dirty
	s_bitset0_b32 s45, 0
	v_mfma_f32_16x16x32_f16 v[198:201], v[152:155], v[16:19], 0
	v_mfma_f32_16x16x32_f16 v[202:205], v[48:51], v[16:19], 0
	v_mfma_f32_16x16x32_f16 v[212:215], v[88:91], v[16:19], 0
	v_mfma_f32_16x16x32_f16 v[216:219], v[92:95], v[16:19], 0
	v_mfma_f32_16x16x32_f16 v[220:223], v[108:111], v[16:19], 0
	v_mfma_f32_16x16x32_f16 v[224:227], v[112:115], v[16:19], 0
	v_mfma_f32_16x16x32_f16 v[228:231], v[140:143], v[16:19], 0
	v_mfma_f32_16x16x32_f16 v[232:235], v[32:35], v[16:19], v[160:163]
	s_mov_b32 s46, 1
	s_branch .Lrec_wait
